# attention unit epilogues: output dwords scaled/exchanged/packed four at a time and stored under one lane mask (29 groups)
# baseline (speedup 1.0000x reference)
; __device__ __forceinline__ int crow(int r, int hi) { return (r & 3) + 8 * (r >> 2) + 4 * hi; }
; __device__ __forceinline__ unsigned cvtpk(float lo, float hi) { unsigned r; asm volatile("v_cvt_pk_bf16_f32 %0, %1, %2" : "=v"(r) : "v"(lo), "v"(hi)); return r; }
; template <int mode> __device__ __forceinline__ void attn_unit(const AttnArgs& A, const int b, const int h, const int sub, char* shm, const int wave_) {
;     ...
;         bf16* Ow = A.dpo + ((size_t)slot * NTOK + tok0) * DPW + h * 128;
; #pragma unroll
;         for (int r = 0; r < 16; ++r) { const int orow = crow(r, hi);
; #pragma unroll
;             for (int d0 = 0; d0 < 4; ++d0) { const float v = o[d0][r] * rli[r]; const float vn = xor_get<1>(v);
;                 if ((r32 & 1) == 0) *(unsigned*)(Ow + (size_t)orow * dil * DPW + d0 * 32 + r32) = cvtpk(v, vn); } }
.LBB0_898:
	s_or_b64 exec, exec, s[0:1]
	v_add_u32_e32 v0, s14, v0
	v_lshl_add_u64 v[84:85], v[14:15], 0, v[0:1]
	v_mul_f32_e32 v208, v65, v81
	v_mul_f32_e32 v209, v49, v81
	v_mul_f32_e32 v210, v33, v81
	v_mul_f32_e32 v211, v17, v81
	v_mov_b32_dpp v212, v208 quad_perm:[1,0,3,2] row_mask:0xf bank_mask:0xf bound_ctrl:1
	v_mov_b32_dpp v213, v209 quad_perm:[1,0,3,2] row_mask:0xf bank_mask:0xf bound_ctrl:1
	v_mov_b32_dpp v214, v210 quad_perm:[1,0,3,2] row_mask:0xf bank_mask:0xf bound_ctrl:1
	v_mov_b32_dpp v215, v211 quad_perm:[1,0,3,2] row_mask:0xf bank_mask:0xf bound_ctrl:1
	v_cvt_pk_bf16_f32 v208, v208, v212
	v_cvt_pk_bf16_f32 v209, v209, v213
	v_cvt_pk_bf16_f32 v210, v210, v214
	v_cvt_pk_bf16_f32 v211, v211, v215
	s_and_saveexec_b64 s[0:1], vcc
	global_store_dword v[84:85], v208, off
	global_store_dword v[84:85], v209, off offset:64
	global_store_dword v[84:85], v210, off offset:128
	global_store_dword v[84:85], v211, off offset:192
.LBB0_906:
	s_or_b64 exec, exec, s[0:1]
	v_mul_u32_u24_e32 v0, s14, v150
	v_lshl_add_u64 v[16:17], v[14:15], 0, v[0:1]
	v_mul_f32_e32 v208, v66, v82
	v_mul_f32_e32 v209, v50, v82
	v_mul_f32_e32 v210, v34, v82
	v_mul_f32_e32 v211, v18, v82
	v_mov_b32_dpp v212, v208 quad_perm:[1,0,3,2] row_mask:0xf bank_mask:0xf bound_ctrl:1
	v_mov_b32_dpp v213, v209 quad_perm:[1,0,3,2] row_mask:0xf bank_mask:0xf bound_ctrl:1
	v_mov_b32_dpp v214, v210 quad_perm:[1,0,3,2] row_mask:0xf bank_mask:0xf bound_ctrl:1
	v_mov_b32_dpp v215, v211 quad_perm:[1,0,3,2] row_mask:0xf bank_mask:0xf bound_ctrl:1
	v_cvt_pk_bf16_f32 v208, v208, v212
	v_cvt_pk_bf16_f32 v209, v209, v213
	v_cvt_pk_bf16_f32 v210, v210, v214
	v_cvt_pk_bf16_f32 v211, v211, v215
	s_and_saveexec_b64 s[0:1], vcc
	global_store_dword v[16:17], v208, off
	global_store_dword v[16:17], v209, off offset:64
	global_store_dword v[16:17], v210, off offset:128
	global_store_dword v[16:17], v211, off offset:192
.LBB0_914:
	s_or_b64 exec, exec, s[0:1]
	v_mul_u32_u24_e32 v0, s14, v148
	v_lshl_add_u64 v[16:17], v[14:15], 0, v[0:1]
	v_mul_f32_e32 v208, v67, v83
	v_mul_f32_e32 v209, v51, v83
	v_mul_f32_e32 v210, v35, v83
	v_mul_f32_e32 v211, v19, v83
	v_mov_b32_dpp v212, v208 quad_perm:[1,0,3,2] row_mask:0xf bank_mask:0xf bound_ctrl:1
	v_mov_b32_dpp v213, v209 quad_perm:[1,0,3,2] row_mask:0xf bank_mask:0xf bound_ctrl:1
	v_mov_b32_dpp v214, v210 quad_perm:[1,0,3,2] row_mask:0xf bank_mask:0xf bound_ctrl:1
	v_mov_b32_dpp v215, v211 quad_perm:[1,0,3,2] row_mask:0xf bank_mask:0xf bound_ctrl:1
	v_cvt_pk_bf16_f32 v208, v208, v212
	v_cvt_pk_bf16_f32 v209, v209, v213
	v_cvt_pk_bf16_f32 v210, v210, v214
	v_cvt_pk_bf16_f32 v211, v211, v215
	s_and_saveexec_b64 s[0:1], vcc
	global_store_dword v[16:17], v208, off
	global_store_dword v[16:17], v209, off offset:64
	global_store_dword v[16:17], v210, off offset:128
	global_store_dword v[16:17], v211, off offset:192
.LBB0_922:
	s_or_b64 exec, exec, s[0:1]
	v_mul_u32_u24_e32 v0, s14, v146
	v_lshl_add_u64 v[16:17], v[14:15], 0, v[0:1]
	s_waitcnt lgkmcnt(2)
	v_mul_f32_e32 v208, v68, v10
	v_mul_f32_e32 v209, v52, v10
	v_mul_f32_e32 v210, v36, v10
	v_mul_f32_e32 v211, v20, v10
	v_mov_b32_dpp v212, v208 quad_perm:[1,0,3,2] row_mask:0xf bank_mask:0xf bound_ctrl:1
	v_mov_b32_dpp v213, v209 quad_perm:[1,0,3,2] row_mask:0xf bank_mask:0xf bound_ctrl:1
	v_mov_b32_dpp v214, v210 quad_perm:[1,0,3,2] row_mask:0xf bank_mask:0xf bound_ctrl:1
	v_mov_b32_dpp v215, v211 quad_perm:[1,0,3,2] row_mask:0xf bank_mask:0xf bound_ctrl:1
	v_cvt_pk_bf16_f32 v208, v208, v212
	v_cvt_pk_bf16_f32 v209, v209, v213
	v_cvt_pk_bf16_f32 v210, v210, v214
	v_cvt_pk_bf16_f32 v211, v211, v215
	s_and_saveexec_b64 s[0:1], vcc
	global_store_dword v[16:17], v208, off
	global_store_dword v[16:17], v209, off offset:64
	global_store_dword v[16:17], v210, off offset:128
	global_store_dword v[16:17], v211, off offset:192
.LBB0_930:
	s_or_b64 exec, exec, s[0:1]
	v_mul_u32_u24_e32 v0, s14, v143
	v_lshl_add_u64 v[16:17], v[14:15], 0, v[0:1]
	v_mul_f32_e32 v208, v69, v11
	v_mul_f32_e32 v209, v53, v11
	v_mul_f32_e32 v210, v37, v11
	v_mul_f32_e32 v211, v21, v11
	v_mov_b32_dpp v212, v208 quad_perm:[1,0,3,2] row_mask:0xf bank_mask:0xf bound_ctrl:1
	v_mov_b32_dpp v213, v209 quad_perm:[1,0,3,2] row_mask:0xf bank_mask:0xf bound_ctrl:1
	v_mov_b32_dpp v214, v210 quad_perm:[1,0,3,2] row_mask:0xf bank_mask:0xf bound_ctrl:1
	v_mov_b32_dpp v215, v211 quad_perm:[1,0,3,2] row_mask:0xf bank_mask:0xf bound_ctrl:1
	v_cvt_pk_bf16_f32 v208, v208, v212
	v_cvt_pk_bf16_f32 v209, v209, v213
	v_cvt_pk_bf16_f32 v210, v210, v214
	v_cvt_pk_bf16_f32 v211, v211, v215
	s_and_saveexec_b64 s[0:1], vcc
	global_store_dword v[16:17], v208, off
	global_store_dword v[16:17], v209, off offset:64
	global_store_dword v[16:17], v210, off offset:128
	global_store_dword v[16:17], v211, off offset:192
.LBB0_938:
	s_or_b64 exec, exec, s[0:1]
	v_mul_u32_u24_e32 v0, s14, v141
	v_lshl_add_u64 v[10:11], v[14:15], 0, v[0:1]
	v_mul_f32_e32 v208, v70, v12
	v_mul_f32_e32 v209, v54, v12
	v_mul_f32_e32 v210, v38, v12
	v_mul_f32_e32 v211, v22, v12
	v_mov_b32_dpp v212, v208 quad_perm:[1,0,3,2] row_mask:0xf bank_mask:0xf bound_ctrl:1
	v_mov_b32_dpp v213, v209 quad_perm:[1,0,3,2] row_mask:0xf bank_mask:0xf bound_ctrl:1
	v_mov_b32_dpp v214, v210 quad_perm:[1,0,3,2] row_mask:0xf bank_mask:0xf bound_ctrl:1
	v_mov_b32_dpp v215, v211 quad_perm:[1,0,3,2] row_mask:0xf bank_mask:0xf bound_ctrl:1
	v_cvt_pk_bf16_f32 v208, v208, v212
	v_cvt_pk_bf16_f32 v209, v209, v213
	v_cvt_pk_bf16_f32 v210, v210, v214
	v_cvt_pk_bf16_f32 v211, v211, v215
	s_and_saveexec_b64 s[0:1], vcc
	global_store_dword v[10:11], v208, off
	global_store_dword v[10:11], v209, off offset:64
	global_store_dword v[10:11], v210, off offset:128
	global_store_dword v[10:11], v211, off offset:192
; __device__ __forceinline__ int crow(int r, int hi) { return (r & 3) + 8 * (r >> 2) + 4 * hi; }
; __device__ __forceinline__ unsigned cvtpk(float lo, float hi) { unsigned r; asm volatile("v_cvt_pk_bf16_f32 %0, %1, %2" : "=v"(r) : "v"(lo), "v"(hi)); return r; }
; template <int mode> __device__ __forceinline__ void attn_unit(const AttnArgs& A, const int b, const int h, const int sub, char* shm, const int wave_) {
;     ...
;         bf16* Ow = A.dpo + ((size_t)slot * NTOK + tok0) * DPW + h * 128;
; #pragma unroll
;         for (int r = 0; r < 16; ++r) { const int orow = crow(r, hi);
; #pragma unroll
;             for (int d0 = 0; d0 < 4; ++d0) { const float v = o[d0][r] * rli[r]; const float vn = xor_get<1>(v);
;                 if ((r32 & 1) == 0) *(unsigned*)(Ow + (size_t)orow * dil * DPW + d0 * 32 + r32) = cvtpk(v, vn); } }
.LBB0_946:
	s_or_b64 exec, exec, s[0:1]
	v_mul_u32_u24_e32 v0, s14, v140
	v_lshl_add_u64 v[10:11], v[14:15], 0, v[0:1]
	v_mul_f32_e32 v208, v71, v13
	v_mul_f32_e32 v209, v55, v13
	v_mul_f32_e32 v210, v39, v13
	v_mul_f32_e32 v211, v23, v13
	v_mov_b32_dpp v212, v208 quad_perm:[1,0,3,2] row_mask:0xf bank_mask:0xf bound_ctrl:1
	v_mov_b32_dpp v213, v209 quad_perm:[1,0,3,2] row_mask:0xf bank_mask:0xf bound_ctrl:1
	v_mov_b32_dpp v214, v210 quad_perm:[1,0,3,2] row_mask:0xf bank_mask:0xf bound_ctrl:1
	v_mov_b32_dpp v215, v211 quad_perm:[1,0,3,2] row_mask:0xf bank_mask:0xf bound_ctrl:1
	v_cvt_pk_bf16_f32 v208, v208, v212
	v_cvt_pk_bf16_f32 v209, v209, v213
	v_cvt_pk_bf16_f32 v210, v210, v214
	v_cvt_pk_bf16_f32 v211, v211, v215
	s_and_saveexec_b64 s[0:1], vcc
	global_store_dword v[10:11], v208, off
	global_store_dword v[10:11], v209, off offset:64
	global_store_dword v[10:11], v210, off offset:128
	global_store_dword v[10:11], v211, off offset:192
.LBB0_954:
	s_or_b64 exec, exec, s[0:1]
	v_mul_u32_u24_e32 v0, s14, v139
	v_lshl_add_u64 v[10:11], v[14:15], 0, v[0:1]
	s_waitcnt lgkmcnt(1)
	v_mul_f32_e32 v208, v72, v6
	v_mul_f32_e32 v209, v56, v6
	v_mul_f32_e32 v210, v40, v6
	v_mul_f32_e32 v211, v24, v6
	v_mov_b32_dpp v212, v208 quad_perm:[1,0,3,2] row_mask:0xf bank_mask:0xf bound_ctrl:1
	v_mov_b32_dpp v213, v209 quad_perm:[1,0,3,2] row_mask:0xf bank_mask:0xf bound_ctrl:1
	v_mov_b32_dpp v214, v210 quad_perm:[1,0,3,2] row_mask:0xf bank_mask:0xf bound_ctrl:1
	v_mov_b32_dpp v215, v211 quad_perm:[1,0,3,2] row_mask:0xf bank_mask:0xf bound_ctrl:1
	v_cvt_pk_bf16_f32 v208, v208, v212
	v_cvt_pk_bf16_f32 v209, v209, v213
	v_cvt_pk_bf16_f32 v210, v210, v214
	v_cvt_pk_bf16_f32 v211, v211, v215
	s_and_saveexec_b64 s[0:1], vcc
	global_store_dword v[10:11], v208, off
	global_store_dword v[10:11], v209, off offset:64
	global_store_dword v[10:11], v210, off offset:128
	global_store_dword v[10:11], v211, off offset:192
.LBB0_962:
	s_or_b64 exec, exec, s[0:1]
	v_mul_u32_u24_e32 v0, s14, v138
	v_lshl_add_u64 v[10:11], v[14:15], 0, v[0:1]
	v_mul_f32_e32 v208, v73, v7
	v_mul_f32_e32 v209, v57, v7
	v_mul_f32_e32 v210, v41, v7
	v_mul_f32_e32 v211, v25, v7
	v_mov_b32_dpp v212, v208 quad_perm:[1,0,3,2] row_mask:0xf bank_mask:0xf bound_ctrl:1
	v_mov_b32_dpp v213, v209 quad_perm:[1,0,3,2] row_mask:0xf bank_mask:0xf bound_ctrl:1
	v_mov_b32_dpp v214, v210 quad_perm:[1,0,3,2] row_mask:0xf bank_mask:0xf bound_ctrl:1
	v_mov_b32_dpp v215, v211 quad_perm:[1,0,3,2] row_mask:0xf bank_mask:0xf bound_ctrl:1
	v_cvt_pk_bf16_f32 v208, v208, v212
	v_cvt_pk_bf16_f32 v209, v209, v213
	v_cvt_pk_bf16_f32 v210, v210, v214
	v_cvt_pk_bf16_f32 v211, v211, v215
	s_and_saveexec_b64 s[0:1], vcc
	global_store_dword v[10:11], v208, off
	global_store_dword v[10:11], v209, off offset:64
	global_store_dword v[10:11], v210, off offset:128
	global_store_dword v[10:11], v211, off offset:192
.LBB0_970:
	s_or_b64 exec, exec, s[0:1]
	v_mul_u32_u24_e32 v0, s14, v137
	v_lshl_add_u64 v[6:7], v[14:15], 0, v[0:1]
	v_mul_f32_e32 v208, v74, v8
	v_mul_f32_e32 v209, v58, v8
	v_mul_f32_e32 v210, v42, v8
	v_mul_f32_e32 v211, v26, v8
	v_mov_b32_dpp v212, v208 quad_perm:[1,0,3,2] row_mask:0xf bank_mask:0xf bound_ctrl:1
	v_mov_b32_dpp v213, v209 quad_perm:[1,0,3,2] row_mask:0xf bank_mask:0xf bound_ctrl:1
	v_mov_b32_dpp v214, v210 quad_perm:[1,0,3,2] row_mask:0xf bank_mask:0xf bound_ctrl:1
	v_mov_b32_dpp v215, v211 quad_perm:[1,0,3,2] row_mask:0xf bank_mask:0xf bound_ctrl:1
	v_cvt_pk_bf16_f32 v208, v208, v212
	v_cvt_pk_bf16_f32 v209, v209, v213
	v_cvt_pk_bf16_f32 v210, v210, v214
	v_cvt_pk_bf16_f32 v211, v211, v215
	s_and_saveexec_b64 s[0:1], vcc
	global_store_dword v[6:7], v208, off
	global_store_dword v[6:7], v209, off offset:64
	global_store_dword v[6:7], v210, off offset:128
	global_store_dword v[6:7], v211, off offset:192
; __device__ __forceinline__ int crow(int r, int hi) { return (r & 3) + 8 * (r >> 2) + 4 * hi; }
; __device__ __forceinline__ unsigned cvtpk(float lo, float hi) { unsigned r; asm volatile("v_cvt_pk_bf16_f32 %0, %1, %2" : "=v"(r) : "v"(lo), "v"(hi)); return r; }
; template <int mode> __device__ __forceinline__ void attn_unit(const AttnArgs& A, const int b, const int h, const int sub, char* shm, const int wave_) {
;     ...
;         bf16* Ow = A.dpo + ((size_t)slot * NTOK + tok0) * DPW + h * 128;
; #pragma unroll
;         for (int r = 0; r < 16; ++r) { const int orow = crow(r, hi);
; #pragma unroll
;             for (int d0 = 0; d0 < 4; ++d0) { const float v = o[d0][r] * rli[r]; const float vn = xor_get<1>(v);
;                 if ((r32 & 1) == 0) *(unsigned*)(Ow + (size_t)orow * dil * DPW + d0 * 32 + r32) = cvtpk(v, vn); } }
.LBB0_978:
	s_or_b64 exec, exec, s[0:1]
	v_mul_u32_u24_e32 v0, s14, v136
	v_lshl_add_u64 v[6:7], v[14:15], 0, v[0:1]
	v_mul_f32_e32 v208, v75, v9
	v_mul_f32_e32 v209, v59, v9
	v_mul_f32_e32 v210, v43, v9
	v_mul_f32_e32 v211, v27, v9
	v_mov_b32_dpp v212, v208 quad_perm:[1,0,3,2] row_mask:0xf bank_mask:0xf bound_ctrl:1
	v_mov_b32_dpp v213, v209 quad_perm:[1,0,3,2] row_mask:0xf bank_mask:0xf bound_ctrl:1
	v_mov_b32_dpp v214, v210 quad_perm:[1,0,3,2] row_mask:0xf bank_mask:0xf bound_ctrl:1
	v_mov_b32_dpp v215, v211 quad_perm:[1,0,3,2] row_mask:0xf bank_mask:0xf bound_ctrl:1
	v_cvt_pk_bf16_f32 v208, v208, v212
	v_cvt_pk_bf16_f32 v209, v209, v213
	v_cvt_pk_bf16_f32 v210, v210, v214
	v_cvt_pk_bf16_f32 v211, v211, v215
	s_and_saveexec_b64 s[0:1], vcc
	global_store_dword v[6:7], v208, off
	global_store_dword v[6:7], v209, off offset:64
	global_store_dword v[6:7], v210, off offset:128
	global_store_dword v[6:7], v211, off offset:192
.LBB0_986:
	s_or_b64 exec, exec, s[0:1]
	v_mul_u32_u24_e32 v0, s14, v135
	v_lshl_add_u64 v[6:7], v[14:15], 0, v[0:1]
	s_waitcnt lgkmcnt(0)
	v_mul_f32_e32 v208, v76, v2
	v_mul_f32_e32 v209, v60, v2
	v_mul_f32_e32 v210, v44, v2
	v_mul_f32_e32 v211, v28, v2
	v_mov_b32_dpp v212, v208 quad_perm:[1,0,3,2] row_mask:0xf bank_mask:0xf bound_ctrl:1
	v_mov_b32_dpp v213, v209 quad_perm:[1,0,3,2] row_mask:0xf bank_mask:0xf bound_ctrl:1
	v_mov_b32_dpp v214, v210 quad_perm:[1,0,3,2] row_mask:0xf bank_mask:0xf bound_ctrl:1
	v_mov_b32_dpp v215, v211 quad_perm:[1,0,3,2] row_mask:0xf bank_mask:0xf bound_ctrl:1
	v_cvt_pk_bf16_f32 v208, v208, v212
	v_cvt_pk_bf16_f32 v209, v209, v213
	v_cvt_pk_bf16_f32 v210, v210, v214
	v_cvt_pk_bf16_f32 v211, v211, v215
	s_and_saveexec_b64 s[0:1], vcc
	global_store_dword v[6:7], v208, off
	global_store_dword v[6:7], v209, off offset:64
	global_store_dword v[6:7], v210, off offset:128
	global_store_dword v[6:7], v211, off offset:192
.LBB0_994:
	s_or_b64 exec, exec, s[0:1]
	v_mul_u32_u24_e32 v0, s14, v134
	v_lshl_add_u64 v[6:7], v[14:15], 0, v[0:1]
	v_mul_f32_e32 v208, v77, v3
	v_mul_f32_e32 v209, v61, v3
	v_mul_f32_e32 v210, v45, v3
	v_mul_f32_e32 v211, v29, v3
	v_mov_b32_dpp v212, v208 quad_perm:[1,0,3,2] row_mask:0xf bank_mask:0xf bound_ctrl:1
	v_mov_b32_dpp v213, v209 quad_perm:[1,0,3,2] row_mask:0xf bank_mask:0xf bound_ctrl:1
	v_mov_b32_dpp v214, v210 quad_perm:[1,0,3,2] row_mask:0xf bank_mask:0xf bound_ctrl:1
	v_mov_b32_dpp v215, v211 quad_perm:[1,0,3,2] row_mask:0xf bank_mask:0xf bound_ctrl:1
	v_cvt_pk_bf16_f32 v208, v208, v212
	v_cvt_pk_bf16_f32 v209, v209, v213
	v_cvt_pk_bf16_f32 v210, v210, v214
	v_cvt_pk_bf16_f32 v211, v211, v215
	s_and_saveexec_b64 s[0:1], vcc
	global_store_dword v[6:7], v208, off
	global_store_dword v[6:7], v209, off offset:64
	global_store_dword v[6:7], v210, off offset:128
	global_store_dword v[6:7], v211, off offset:192
.LBB0_1002:
	s_or_b64 exec, exec, s[0:1]
	v_mul_u32_u24_e32 v0, s14, v132
	v_lshl_add_u64 v[2:3], v[14:15], 0, v[0:1]
	v_mul_f32_e32 v208, v78, v4
	v_mul_f32_e32 v209, v62, v4
	v_mul_f32_e32 v210, v46, v4
	v_mul_f32_e32 v211, v30, v4
	v_mov_b32_dpp v212, v208 quad_perm:[1,0,3,2] row_mask:0xf bank_mask:0xf bound_ctrl:1
	v_mov_b32_dpp v213, v209 quad_perm:[1,0,3,2] row_mask:0xf bank_mask:0xf bound_ctrl:1
	v_mov_b32_dpp v214, v210 quad_perm:[1,0,3,2] row_mask:0xf bank_mask:0xf bound_ctrl:1
	v_mov_b32_dpp v215, v211 quad_perm:[1,0,3,2] row_mask:0xf bank_mask:0xf bound_ctrl:1
	v_cvt_pk_bf16_f32 v208, v208, v212
	v_cvt_pk_bf16_f32 v209, v209, v213
	v_cvt_pk_bf16_f32 v210, v210, v214
	v_cvt_pk_bf16_f32 v211, v211, v215
	s_and_saveexec_b64 s[0:1], vcc
	global_store_dword v[2:3], v208, off
	global_store_dword v[2:3], v209, off offset:64
	global_store_dword v[2:3], v210, off offset:128
	global_store_dword v[2:3], v211, off offset:192

; __device__ __forceinline__ int crow(int r, int hi) { return (r & 3) + 8 * (r >> 2) + 4 * hi; }
; __device__ __forceinline__ unsigned cvtpk(float lo, float hi) { unsigned r; asm volatile("v_cvt_pk_bf16_f32 %0, %1, %2" : "=v"(r) : "v"(lo), "v"(hi)); return r; }
; template <int mode> __device__ __forceinline__ void attn_unit(const AttnArgs& A, const int b, const int h, const int sub, char* shm, const int wave_) {
;     ...
;         asm volatile("s_waitcnt lgkmcnt(0)" ::: "memory");
;         float rli[16];
; #pragma unroll
;         for (int r = 0; r < 16; ++r) rli[r] = li_l[crow(r, hi)];
;         if (mode == 3) {
; #pragma unroll
;             for (int r = 0; r < 16; ++r) { const int ts = ts_l[crow(r, hi)]; bf16* Ow = A.dpo + (size_t)(ts < 0 ? 0 : ts) * DPW + h * 128;
; #pragma unroll
;                 for (int d0 = 0; d0 < 4; ++d0) { const float v = o[d0][r] * rli[r]; const float vn = xor_get<1>(v);
;                     if ((r32 & 1) == 0 && ts >= 0) *(unsigned*)(Ow + d0 * 32 + r32) = cvtpk(v, vn); } }
;         } else {
;         bf16* Ow = A.dpo + ((size_t)slot * NTOK + tok0) * DPW + h * 128;
; #pragma unroll
;         for (int r = 0; r < 16; ++r) { const int orow = crow(r, hi);
; #pragma unroll
;             for (int d0 = 0; d0 < 4; ++d0) { const float v = o[d0][r] * rli[r]; const float vn = xor_get<1>(v);
;                 if ((r32 & 1) == 0) *(unsigned*)(Ow + (size_t)orow * dil * DPW + d0 * 32 + r32) = cvtpk(v, vn); } }
.LBB0_1030:
	s_or_b64 exec, exec, s[0:1]
	s_mul_hi_u32 s0, s27, 0xb00
	s_mulk_i32 s27, 0xb00
	s_add_u32 s1, s92, s27
	s_addc_u32 s14, s93, s0
	s_waitcnt lgkmcnt(0)
	s_add_u32 s0, s1, s28
	ds_read_b128 v[78:81], v137
	ds_read_b128 v[74:77], v137 offset:32
	ds_read_b128 v[70:73], v137 offset:64
	ds_read_b128 v[66:69], v137 offset:96
	s_addc_u32 s1, s14, 0
	v_and_b32_e32 v0, 1, v134
	v_cmp_eq_u32_e32 vcc, 0, v0
	v_lshl_add_u64 v[82:83], v[126:127], 1, s[0:1]
	v_mul_u32_u24_e32 v0, 0x2c00, v135
	v_lshl_add_u64 v[84:85], v[82:83], 0, v[0:1]
	s_waitcnt lgkmcnt(3)
	v_mul_f32_e32 v208, v50, v78
	v_mul_f32_e32 v209, v34, v78
	v_mul_f32_e32 v210, v18, v78
	v_mul_f32_e32 v211, v2, v78
	v_mov_b32_dpp v212, v208 quad_perm:[1,0,3,2] row_mask:0xf bank_mask:0xf bound_ctrl:1
	v_mov_b32_dpp v213, v209 quad_perm:[1,0,3,2] row_mask:0xf bank_mask:0xf bound_ctrl:1
	v_mov_b32_dpp v214, v210 quad_perm:[1,0,3,2] row_mask:0xf bank_mask:0xf bound_ctrl:1
	v_mov_b32_dpp v215, v211 quad_perm:[1,0,3,2] row_mask:0xf bank_mask:0xf bound_ctrl:1
	v_cvt_pk_bf16_f32 v208, v208, v212
	v_cvt_pk_bf16_f32 v209, v209, v213
	v_cvt_pk_bf16_f32 v210, v210, v214
	v_cvt_pk_bf16_f32 v211, v211, v215
	s_and_saveexec_b64 s[0:1], vcc
	global_store_dword v[84:85], v208, off
	global_store_dword v[84:85], v209, off offset:64
	global_store_dword v[84:85], v210, off offset:128
	global_store_dword v[84:85], v211, off offset:192
.LBB0_1038:
	s_or_b64 exec, exec, s[0:1]
	v_mul_u32_u24_e32 v0, 0xb00, v136
	v_lshl_add_u64 v[84:85], v[82:83], 0, v[0:1]
	v_mul_f32_e32 v208, v51, v79
	v_mul_f32_e32 v209, v35, v79
	v_mul_f32_e32 v210, v19, v79
	v_mul_f32_e32 v211, v3, v79
	v_mov_b32_dpp v212, v208 quad_perm:[1,0,3,2] row_mask:0xf bank_mask:0xf bound_ctrl:1
	v_mov_b32_dpp v213, v209 quad_perm:[1,0,3,2] row_mask:0xf bank_mask:0xf bound_ctrl:1
	v_mov_b32_dpp v214, v210 quad_perm:[1,0,3,2] row_mask:0xf bank_mask:0xf bound_ctrl:1
	v_mov_b32_dpp v215, v211 quad_perm:[1,0,3,2] row_mask:0xf bank_mask:0xf bound_ctrl:1
	v_cvt_pk_bf16_f32 v208, v208, v212
	v_cvt_pk_bf16_f32 v209, v209, v213
	v_cvt_pk_bf16_f32 v210, v210, v214
	v_cvt_pk_bf16_f32 v211, v211, v215
	s_and_saveexec_b64 s[0:1], vcc
	global_store_dword v[84:85], v208, off
	global_store_dword v[84:85], v209, off offset:64
	global_store_dword v[84:85], v210, off offset:128
	global_store_dword v[84:85], v211, off offset:192
.LBB0_1046:
	s_or_b64 exec, exec, s[0:1]
	v_mul_u32_u24_e32 v0, 0xb00, v128
	v_lshl_add_u64 v[2:3], v[82:83], 0, v[0:1]
	v_mul_f32_e32 v208, v52, v80
	v_mul_f32_e32 v209, v36, v80
	v_mul_f32_e32 v210, v20, v80
	v_mul_f32_e32 v211, v4, v80
	v_mov_b32_dpp v212, v208 quad_perm:[1,0,3,2] row_mask:0xf bank_mask:0xf bound_ctrl:1
	v_mov_b32_dpp v213, v209 quad_perm:[1,0,3,2] row_mask:0xf bank_mask:0xf bound_ctrl:1
	v_mov_b32_dpp v214, v210 quad_perm:[1,0,3,2] row_mask:0xf bank_mask:0xf bound_ctrl:1
	v_mov_b32_dpp v215, v211 quad_perm:[1,0,3,2] row_mask:0xf bank_mask:0xf bound_ctrl:1
	v_cvt_pk_bf16_f32 v208, v208, v212
	v_cvt_pk_bf16_f32 v209, v209, v213
	v_cvt_pk_bf16_f32 v210, v210, v214
	v_cvt_pk_bf16_f32 v211, v211, v215
	s_and_saveexec_b64 s[0:1], vcc
	global_store_dword v[2:3], v208, off
	global_store_dword v[2:3], v209, off offset:64
	global_store_dword v[2:3], v210, off offset:128
	global_store_dword v[2:3], v211, off offset:192
.LBB0_1054:
	s_or_b64 exec, exec, s[0:1]
	v_mul_u32_u24_e32 v0, 0xb00, v129
	v_lshl_add_u64 v[2:3], v[82:83], 0, v[0:1]
	v_mul_f32_e32 v208, v53, v81
	v_mul_f32_e32 v209, v37, v81
	v_mul_f32_e32 v210, v21, v81
	v_mul_f32_e32 v211, v5, v81
	v_mov_b32_dpp v212, v208 quad_perm:[1,0,3,2] row_mask:0xf bank_mask:0xf bound_ctrl:1
	v_mov_b32_dpp v213, v209 quad_perm:[1,0,3,2] row_mask:0xf bank_mask:0xf bound_ctrl:1
	v_mov_b32_dpp v214, v210 quad_perm:[1,0,3,2] row_mask:0xf bank_mask:0xf bound_ctrl:1
	v_mov_b32_dpp v215, v211 quad_perm:[1,0,3,2] row_mask:0xf bank_mask:0xf bound_ctrl:1
	v_cvt_pk_bf16_f32 v208, v208, v212
	v_cvt_pk_bf16_f32 v209, v209, v213
	v_cvt_pk_bf16_f32 v210, v210, v214
	v_cvt_pk_bf16_f32 v211, v211, v215
	s_and_saveexec_b64 s[0:1], vcc
	global_store_dword v[2:3], v208, off
	global_store_dword v[2:3], v209, off offset:64
	global_store_dword v[2:3], v210, off offset:128
	global_store_dword v[2:3], v211, off offset:192
.LBB0_1062:
	s_or_b64 exec, exec, s[0:1]
	v_mul_u32_u24_e32 v0, 0xb00, v124
	v_lshl_add_u64 v[2:3], v[82:83], 0, v[0:1]
	s_waitcnt lgkmcnt(2)
	v_mul_f32_e32 v208, v54, v74
	v_mul_f32_e32 v209, v38, v74
	v_mul_f32_e32 v210, v22, v74
	v_mul_f32_e32 v211, v6, v74
	v_mov_b32_dpp v212, v208 quad_perm:[1,0,3,2] row_mask:0xf bank_mask:0xf bound_ctrl:1
	v_mov_b32_dpp v213, v209 quad_perm:[1,0,3,2] row_mask:0xf bank_mask:0xf bound_ctrl:1
	v_mov_b32_dpp v214, v210 quad_perm:[1,0,3,2] row_mask:0xf bank_mask:0xf bound_ctrl:1
	v_mov_b32_dpp v215, v211 quad_perm:[1,0,3,2] row_mask:0xf bank_mask:0xf bound_ctrl:1
	v_cvt_pk_bf16_f32 v208, v208, v212
	v_cvt_pk_bf16_f32 v209, v209, v213
	v_cvt_pk_bf16_f32 v210, v210, v214
	v_cvt_pk_bf16_f32 v211, v211, v215
	s_and_saveexec_b64 s[0:1], vcc
	global_store_dword v[2:3], v208, off
	global_store_dword v[2:3], v209, off offset:64
	global_store_dword v[2:3], v210, off offset:128
	global_store_dword v[2:3], v211, off offset:192
; __device__ __forceinline__ int crow(int r, int hi) { return (r & 3) + 8 * (r >> 2) + 4 * hi; }
; __device__ __forceinline__ unsigned cvtpk(float lo, float hi) { unsigned r; asm volatile("v_cvt_pk_bf16_f32 %0, %1, %2" : "=v"(r) : "v"(lo), "v"(hi)); return r; }
; template <int mode> __device__ __forceinline__ void attn_unit(const AttnArgs& A, const int b, const int h, const int sub, char* shm, const int wave_) {
;     ...
;         bf16* Ow = A.dpo + ((size_t)slot * NTOK + tok0) * DPW + h * 128;
; #pragma unroll
;         for (int r = 0; r < 16; ++r) { const int orow = crow(r, hi);
; #pragma unroll
;             for (int d0 = 0; d0 < 4; ++d0) { const float v = o[d0][r] * rli[r]; const float vn = xor_get<1>(v);
;                 if ((r32 & 1) == 0) *(unsigned*)(Ow + (size_t)orow * dil * DPW + d0 * 32 + r32) = cvtpk(v, vn); } }
.LBB0_1070:
	s_or_b64 exec, exec, s[0:1]
	v_mul_u32_u24_e32 v0, 0xb00, v125
	v_lshl_add_u64 v[2:3], v[82:83], 0, v[0:1]
	v_mul_f32_e32 v208, v55, v75
	v_mul_f32_e32 v209, v39, v75
	v_mul_f32_e32 v210, v23, v75
	v_mul_f32_e32 v211, v7, v75
	v_mov_b32_dpp v212, v208 quad_perm:[1,0,3,2] row_mask:0xf bank_mask:0xf bound_ctrl:1
	v_mov_b32_dpp v213, v209 quad_perm:[1,0,3,2] row_mask:0xf bank_mask:0xf bound_ctrl:1
	v_mov_b32_dpp v214, v210 quad_perm:[1,0,3,2] row_mask:0xf bank_mask:0xf bound_ctrl:1
	v_mov_b32_dpp v215, v211 quad_perm:[1,0,3,2] row_mask:0xf bank_mask:0xf bound_ctrl:1
	v_cvt_pk_bf16_f32 v208, v208, v212
	v_cvt_pk_bf16_f32 v209, v209, v213
	v_cvt_pk_bf16_f32 v210, v210, v214
	v_cvt_pk_bf16_f32 v211, v211, v215
	s_and_saveexec_b64 s[0:1], vcc
	global_store_dword v[2:3], v208, off
	global_store_dword v[2:3], v209, off offset:64
	global_store_dword v[2:3], v210, off offset:128
	global_store_dword v[2:3], v211, off offset:192
.LBB0_1078:
	s_or_b64 exec, exec, s[0:1]
	v_mul_u32_u24_e32 v0, 0xb00, v122
	v_lshl_add_u64 v[2:3], v[82:83], 0, v[0:1]
	v_mul_f32_e32 v208, v56, v76
	v_mul_f32_e32 v209, v40, v76
	v_mul_f32_e32 v210, v24, v76
	v_mul_f32_e32 v211, v8, v76
	v_mov_b32_dpp v212, v208 quad_perm:[1,0,3,2] row_mask:0xf bank_mask:0xf bound_ctrl:1
	v_mov_b32_dpp v213, v209 quad_perm:[1,0,3,2] row_mask:0xf bank_mask:0xf bound_ctrl:1
	v_mov_b32_dpp v214, v210 quad_perm:[1,0,3,2] row_mask:0xf bank_mask:0xf bound_ctrl:1
	v_mov_b32_dpp v215, v211 quad_perm:[1,0,3,2] row_mask:0xf bank_mask:0xf bound_ctrl:1
	v_cvt_pk_bf16_f32 v208, v208, v212
	v_cvt_pk_bf16_f32 v209, v209, v213
	v_cvt_pk_bf16_f32 v210, v210, v214
	v_cvt_pk_bf16_f32 v211, v211, v215
	s_and_saveexec_b64 s[0:1], vcc
	global_store_dword v[2:3], v208, off
	global_store_dword v[2:3], v209, off offset:64
	global_store_dword v[2:3], v210, off offset:128
	global_store_dword v[2:3], v211, off offset:192
.LBB0_1086:
	s_or_b64 exec, exec, s[0:1]
	v_mul_u32_u24_e32 v0, 0xb00, v123
	v_lshl_add_u64 v[2:3], v[82:83], 0, v[0:1]
	v_mul_f32_e32 v208, v57, v77
	v_mul_f32_e32 v209, v41, v77
	v_mul_f32_e32 v210, v25, v77
	v_mul_f32_e32 v211, v9, v77
	v_mov_b32_dpp v212, v208 quad_perm:[1,0,3,2] row_mask:0xf bank_mask:0xf bound_ctrl:1
	v_mov_b32_dpp v213, v209 quad_perm:[1,0,3,2] row_mask:0xf bank_mask:0xf bound_ctrl:1
	v_mov_b32_dpp v214, v210 quad_perm:[1,0,3,2] row_mask:0xf bank_mask:0xf bound_ctrl:1
	v_mov_b32_dpp v215, v211 quad_perm:[1,0,3,2] row_mask:0xf bank_mask:0xf bound_ctrl:1
	v_cvt_pk_bf16_f32 v208, v208, v212
	v_cvt_pk_bf16_f32 v209, v209, v213
	v_cvt_pk_bf16_f32 v210, v210, v214
	v_cvt_pk_bf16_f32 v211, v211, v215
	s_and_saveexec_b64 s[0:1], vcc
	global_store_dword v[2:3], v208, off
	global_store_dword v[2:3], v209, off offset:64
	global_store_dword v[2:3], v210, off offset:128
	global_store_dword v[2:3], v211, off offset:192
.LBB0_1094:
	s_or_b64 exec, exec, s[0:1]
	v_mul_u32_u24_e32 v0, 0xb00, v120
	v_lshl_add_u64 v[2:3], v[82:83], 0, v[0:1]
	s_waitcnt lgkmcnt(1)
	v_mul_f32_e32 v208, v58, v70
	v_mul_f32_e32 v209, v42, v70
	v_mul_f32_e32 v210, v26, v70
	v_mul_f32_e32 v211, v10, v70
	v_mov_b32_dpp v212, v208 quad_perm:[1,0,3,2] row_mask:0xf bank_mask:0xf bound_ctrl:1
	v_mov_b32_dpp v213, v209 quad_perm:[1,0,3,2] row_mask:0xf bank_mask:0xf bound_ctrl:1
	v_mov_b32_dpp v214, v210 quad_perm:[1,0,3,2] row_mask:0xf bank_mask:0xf bound_ctrl:1
	v_mov_b32_dpp v215, v211 quad_perm:[1,0,3,2] row_mask:0xf bank_mask:0xf bound_ctrl:1
	v_cvt_pk_bf16_f32 v208, v208, v212
	v_cvt_pk_bf16_f32 v209, v209, v213
	v_cvt_pk_bf16_f32 v210, v210, v214
	v_cvt_pk_bf16_f32 v211, v211, v215
	s_and_saveexec_b64 s[0:1], vcc
	global_store_dword v[2:3], v208, off
	global_store_dword v[2:3], v209, off offset:64
	global_store_dword v[2:3], v210, off offset:128
	global_store_dword v[2:3], v211, off offset:192
.LBB0_1102:
	s_or_b64 exec, exec, s[0:1]
	v_mul_u32_u24_e32 v0, 0xb00, v121
	v_lshl_add_u64 v[2:3], v[82:83], 0, v[0:1]
	v_mul_f32_e32 v208, v59, v71
	v_mul_f32_e32 v209, v43, v71
	v_mul_f32_e32 v210, v27, v71
	v_mul_f32_e32 v211, v11, v71
	v_mov_b32_dpp v212, v208 quad_perm:[1,0,3,2] row_mask:0xf bank_mask:0xf bound_ctrl:1
	v_mov_b32_dpp v213, v209 quad_perm:[1,0,3,2] row_mask:0xf bank_mask:0xf bound_ctrl:1
	v_mov_b32_dpp v214, v210 quad_perm:[1,0,3,2] row_mask:0xf bank_mask:0xf bound_ctrl:1
	v_mov_b32_dpp v215, v211 quad_perm:[1,0,3,2] row_mask:0xf bank_mask:0xf bound_ctrl:1
	v_cvt_pk_bf16_f32 v208, v208, v212
	v_cvt_pk_bf16_f32 v209, v209, v213
	v_cvt_pk_bf16_f32 v210, v210, v214
	v_cvt_pk_bf16_f32 v211, v211, v215
	s_and_saveexec_b64 s[0:1], vcc
	global_store_dword v[2:3], v208, off
	global_store_dword v[2:3], v209, off offset:64
	global_store_dword v[2:3], v210, off offset:128
	global_store_dword v[2:3], v211, off offset:192
; __device__ __forceinline__ int crow(int r, int hi) { return (r & 3) + 8 * (r >> 2) + 4 * hi; }
; __device__ __forceinline__ unsigned cvtpk(float lo, float hi) { unsigned r; asm volatile("v_cvt_pk_bf16_f32 %0, %1, %2" : "=v"(r) : "v"(lo), "v"(hi)); return r; }
; template <int mode> __device__ __forceinline__ void attn_unit(const AttnArgs& A, const int b, const int h, const int sub, char* shm, const int wave_) {
;     ...
;         bf16* Ow = A.dpo + ((size_t)slot * NTOK + tok0) * DPW + h * 128;
; #pragma unroll
;         for (int r = 0; r < 16; ++r) { const int orow = crow(r, hi);
; #pragma unroll
;             for (int d0 = 0; d0 < 4; ++d0) { const float v = o[d0][r] * rli[r]; const float vn = xor_get<1>(v);
;                 if ((r32 & 1) == 0) *(unsigned*)(Ow + (size_t)orow * dil * DPW + d0 * 32 + r32) = cvtpk(v, vn); } }
.LBB0_1110:
	s_or_b64 exec, exec, s[0:1]
	v_mul_u32_u24_e32 v0, 0xb00, v118
	v_lshl_add_u64 v[2:3], v[82:83], 0, v[0:1]
	v_mul_f32_e32 v208, v60, v72
	v_mul_f32_e32 v209, v44, v72
	v_mul_f32_e32 v210, v28, v72
	v_mul_f32_e32 v211, v12, v72
	v_mov_b32_dpp v212, v208 quad_perm:[1,0,3,2] row_mask:0xf bank_mask:0xf bound_ctrl:1
	v_mov_b32_dpp v213, v209 quad_perm:[1,0,3,2] row_mask:0xf bank_mask:0xf bound_ctrl:1
	v_mov_b32_dpp v214, v210 quad_perm:[1,0,3,2] row_mask:0xf bank_mask:0xf bound_ctrl:1
	v_mov_b32_dpp v215, v211 quad_perm:[1,0,3,2] row_mask:0xf bank_mask:0xf bound_ctrl:1
	v_cvt_pk_bf16_f32 v208, v208, v212
	v_cvt_pk_bf16_f32 v209, v209, v213
	v_cvt_pk_bf16_f32 v210, v210, v214
	v_cvt_pk_bf16_f32 v211, v211, v215
	s_and_saveexec_b64 s[0:1], vcc
	global_store_dword v[2:3], v208, off
	global_store_dword v[2:3], v209, off offset:64
	global_store_dword v[2:3], v210, off offset:128
	global_store_dword v[2:3], v211, off offset:192
.LBB0_1118:
	s_or_b64 exec, exec, s[0:1]
	v_mul_u32_u24_e32 v0, 0xb00, v119
	v_lshl_add_u64 v[2:3], v[82:83], 0, v[0:1]
	v_mul_f32_e32 v208, v61, v73
	v_mul_f32_e32 v209, v45, v73
	v_mul_f32_e32 v210, v29, v73
	v_mul_f32_e32 v211, v13, v73
	v_mov_b32_dpp v212, v208 quad_perm:[1,0,3,2] row_mask:0xf bank_mask:0xf bound_ctrl:1
	v_mov_b32_dpp v213, v209 quad_perm:[1,0,3,2] row_mask:0xf bank_mask:0xf bound_ctrl:1
	v_mov_b32_dpp v214, v210 quad_perm:[1,0,3,2] row_mask:0xf bank_mask:0xf bound_ctrl:1
	v_mov_b32_dpp v215, v211 quad_perm:[1,0,3,2] row_mask:0xf bank_mask:0xf bound_ctrl:1
	v_cvt_pk_bf16_f32 v208, v208, v212
	v_cvt_pk_bf16_f32 v209, v209, v213
	v_cvt_pk_bf16_f32 v210, v210, v214
	v_cvt_pk_bf16_f32 v211, v211, v215
	s_and_saveexec_b64 s[0:1], vcc
	global_store_dword v[2:3], v208, off
	global_store_dword v[2:3], v209, off offset:64
	global_store_dword v[2:3], v210, off offset:128
	global_store_dword v[2:3], v211, off offset:192
.LBB0_1126:
	s_or_b64 exec, exec, s[0:1]
	v_mul_u32_u24_e32 v0, 0xb00, v116
	v_lshl_add_u64 v[2:3], v[82:83], 0, v[0:1]
	s_waitcnt lgkmcnt(0)
	v_mul_f32_e32 v208, v62, v66
	v_mul_f32_e32 v209, v46, v66
	v_mul_f32_e32 v210, v30, v66
	v_mul_f32_e32 v211, v14, v66
	v_mov_b32_dpp v212, v208 quad_perm:[1,0,3,2] row_mask:0xf bank_mask:0xf bound_ctrl:1
	v_mov_b32_dpp v213, v209 quad_perm:[1,0,3,2] row_mask:0xf bank_mask:0xf bound_ctrl:1
	v_mov_b32_dpp v214, v210 quad_perm:[1,0,3,2] row_mask:0xf bank_mask:0xf bound_ctrl:1
	v_mov_b32_dpp v215, v211 quad_perm:[1,0,3,2] row_mask:0xf bank_mask:0xf bound_ctrl:1
	v_cvt_pk_bf16_f32 v208, v208, v212
	v_cvt_pk_bf16_f32 v209, v209, v213
	v_cvt_pk_bf16_f32 v210, v210, v214
	v_cvt_pk_bf16_f32 v211, v211, v215
	s_and_saveexec_b64 s[0:1], vcc
	global_store_dword v[2:3], v208, off
	global_store_dword v[2:3], v209, off offset:64
	global_store_dword v[2:3], v210, off offset:128
	global_store_dword v[2:3], v211, off offset:192
.LBB0_1134:
	s_or_b64 exec, exec, s[0:1]
	v_mul_u32_u24_e32 v0, 0xb00, v117
	v_lshl_add_u64 v[2:3], v[82:83], 0, v[0:1]
	v_mul_f32_e32 v208, v63, v67
	v_mul_f32_e32 v209, v47, v67
	v_mul_f32_e32 v210, v31, v67
	v_mul_f32_e32 v211, v15, v67
	v_mov_b32_dpp v212, v208 quad_perm:[1,0,3,2] row_mask:0xf bank_mask:0xf bound_ctrl:1
	v_mov_b32_dpp v213, v209 quad_perm:[1,0,3,2] row_mask:0xf bank_mask:0xf bound_ctrl:1
	v_mov_b32_dpp v214, v210 quad_perm:[1,0,3,2] row_mask:0xf bank_mask:0xf bound_ctrl:1
	v_mov_b32_dpp v215, v211 quad_perm:[1,0,3,2] row_mask:0xf bank_mask:0xf bound_ctrl:1
	v_cvt_pk_bf16_f32 v208, v208, v212
	v_cvt_pk_bf16_f32 v209, v209, v213
	v_cvt_pk_bf16_f32 v210, v210, v214
	v_cvt_pk_bf16_f32 v211, v211, v215
	s_and_saveexec_b64 s[0:1], vcc
	global_store_dword v[2:3], v208, off
	global_store_dword v[2:3], v209, off offset:64
	global_store_dword v[2:3], v210, off offset:128
	global_store_dword v[2:3], v211, off offset:192
.LBB0_1142:
	s_or_b64 exec, exec, s[0:1]
	v_mul_u32_u24_e32 v0, 0xb00, v114
	v_lshl_add_u64 v[2:3], v[82:83], 0, v[0:1]
	v_mul_f32_e32 v208, v64, v68
	v_mul_f32_e32 v209, v48, v68
	v_mul_f32_e32 v210, v32, v68
	v_mul_f32_e32 v211, v16, v68
	v_mov_b32_dpp v212, v208 quad_perm:[1,0,3,2] row_mask:0xf bank_mask:0xf bound_ctrl:1
	v_mov_b32_dpp v213, v209 quad_perm:[1,0,3,2] row_mask:0xf bank_mask:0xf bound_ctrl:1
	v_mov_b32_dpp v214, v210 quad_perm:[1,0,3,2] row_mask:0xf bank_mask:0xf bound_ctrl:1
	v_mov_b32_dpp v215, v211 quad_perm:[1,0,3,2] row_mask:0xf bank_mask:0xf bound_ctrl:1
	v_cvt_pk_bf16_f32 v208, v208, v212
	v_cvt_pk_bf16_f32 v209, v209, v213
	v_cvt_pk_bf16_f32 v210, v210, v214
	v_cvt_pk_bf16_f32 v211, v211, v215
	s_and_saveexec_b64 s[0:1], vcc
	global_store_dword v[2:3], v208, off
	global_store_dword v[2:3], v209, off offset:64
	global_store_dword v[2:3], v210, off offset:128
	global_store_dword v[2:3], v211, off offset:192
